# P10 bias loaded in the last K-iteration into the dead deferred-store buffer registers (counted waits +4 there); epilogue copies it and drops its vmcnt(0)
# speedup vs baseline: 1.0025x; 1.0025x over previous
.LBB0_1440:
	ds_read_b128 v[18:21], v185
	ds_read_b128 v[22:25], v185 offset:1024
	ds_read_b128 v[26:29], v185 offset:2048
	ds_read_b128 v[30:33], v185 offset:3072
	ds_read_b128 v[2:5], v186
	ds_read_b128 v[6:9], v186 offset:1024
	ds_read_b128 v[10:13], v186 offset:2048
	ds_read_b128 v[14:17], v186 offset:3072
	s_add_u32 s50, s42, 0x80
	s_addc_u32 s51, s43, 0
	s_add_u32 s42, s42, 0x100
	s_addc_u32 s43, s43, 0
	s_add_u32 s44, s44, 0x100
	s_addc_u32 s45, s45, 0
	s_cmp_eq_u32 s37, 12
	s_cselect_b32 s48, s35, s42
	s_cselect_b32 s49, s11, s43
	s_cselect_b32 s46, s8, s44
	s_cselect_b32 s47, s9, s45
	v_lshl_add_u64 v[212:213], s[50:51], 0, v[170:171]
	s_add_i32 m0, s1, 0xc000
	ds_read_b128 v[174:177], v187
	ds_read_b128 v[178:181], v187 offset:1024
	ds_read_b128 v[188:191], v187 offset:2048
	ds_read_b128 v[192:195], v187 offset:3072
	ds_read_b128 v[196:199], v187 offset:4096
	ds_read_b128 v[200:203], v187 offset:5120
	ds_read_b128 v[204:207], v187 offset:6144
	ds_read_b128 v[208:211], v187 offset:7168
	global_load_lds_dwordx4 v[212:213], off
	v_lshl_add_u64 v[212:213], s[50:51], 0, v[172:173]
	s_add_i32 m0, s1, 0xe000
	s_nop 0
	global_load_lds_dwordx4 v[212:213], off
	global_store_dwordx4 v1, v[222:225], s[100:101]
	s_mov_b32 vcc_lo, 0x8000
	s_cmp_eq_u32 s37, 4
	s_cselect_b32 vcc_lo, 0x28000, vcc_lo
	s_add_u32 s100, s100, vcc_lo
	s_addc_u32 s101, s101, 0
	v_mov_b32_e32 v222, v226
	v_mov_b32_e32 v223, v227
	v_mov_b32_e32 v224, v228
	v_mov_b32_e32 v225, v229
	v_mov_b32_e32 v226, v230
	v_mov_b32_e32 v227, v231
	v_mov_b32_e32 v228, v232
	v_mov_b32_e32 v229, v233
	v_mov_b32_e32 v230, v234
	v_mov_b32_e32 v231, v235
	v_mov_b32_e32 v232, v236
	v_mov_b32_e32 v233, v237
	v_mov_b32_e32 v234, v238
	v_mov_b32_e32 v235, v239
	v_mov_b32_e32 v236, v240
	v_mov_b32_e32 v237, v241
	v_mov_b32_e32 v238, v242
	v_mov_b32_e32 v239, v243
	v_mov_b32_e32 v240, v244
	v_mov_b32_e32 v241, v245
	v_mov_b32_e32 v242, v246
	v_mov_b32_e32 v243, v247
	v_mov_b32_e32 v244, v248
	v_mov_b32_e32 v245, v249
	v_mov_b32_e32 v246, v250
	v_mov_b32_e32 v247, v251
	v_mov_b32_e32 v248, v252
	v_mov_b32_e32 v249, v253
	s_waitcnt vmcnt(9)
	s_waitcnt lgkmcnt(0)
	s_barrier
	s_setprio 1
	s_waitcnt lgkmcnt(0)
	v_mfma_f32_16x16x128_f8f6f4 v[158:161], v[18:25], v[174:181], v[158:161]
	v_mfma_f32_16x16x128_f8f6f4 v[154:157], v[26:33], v[174:181], v[154:157]
	v_mfma_f32_16x16x128_f8f6f4 v[150:153], v[18:25], v[188:195], v[150:153]
	v_mfma_f32_16x16x128_f8f6f4 v[146:149], v[26:33], v[188:195], v[146:149]
	v_mfma_f32_16x16x128_f8f6f4 v[142:145], v[18:25], v[196:203], v[142:145]
	v_mfma_f32_16x16x128_f8f6f4 v[134:137], v[26:33], v[196:203], v[134:137]
	v_mfma_f32_16x16x128_f8f6f4 v[118:121], v[18:25], v[204:211], v[118:121]
	v_mfma_f32_16x16x128_f8f6f4 v[110:113], v[26:33], v[204:211], v[110:113]
	s_setprio 0
	s_setprio 1
	v_mfma_f32_16x16x128_f8f6f4 v[138:141], v[2:9], v[174:181], v[138:141]
	v_mfma_f32_16x16x128_f8f6f4 v[130:133], v[10:17], v[174:181], v[130:133]
	v_mfma_f32_16x16x128_f8f6f4 v[126:129], v[2:9], v[188:195], v[126:129]
	v_mfma_f32_16x16x128_f8f6f4 v[122:125], v[10:17], v[188:195], v[122:125]
	v_mfma_f32_16x16x128_f8f6f4 v[114:117], v[2:9], v[196:203], v[114:117]
	v_mfma_f32_16x16x128_f8f6f4 v[106:109], v[10:17], v[196:203], v[106:109]
	v_mfma_f32_16x16x128_f8f6f4 v[102:105], v[2:9], v[204:211], v[102:105]
	v_mfma_f32_16x16x128_f8f6f4 v[98:101], v[10:17], v[204:211], v[98:101]
	s_setprio 0
	s_barrier
	s_cmp_lg_u32 s37, 12
	s_cbranch_scc1 .Lp10_nob
	v_lshl_or_b32 v222, s10, 8, v183
	v_mov_b32_e32 v223, s40
	v_lshlrev_b32_e32 v222, 2, v222
	v_lshl_add_u32 v222, v223, 13, v222
	global_load_dwordx4 v[238:241], v222, s[12:13]
	global_load_dwordx4 v[242:245], v222, s[12:13] offset:16
	global_load_dwordx4 v[246:249], v222, s[12:13] offset:128
	global_load_dwordx4 v[250:253], v222, s[12:13] offset:144
.Lp10_nob:
	s_add_i32 s41, s80, s56
	v_lshl_add_u64 v[174:175], s[46:47], 0, v[164:165]
	s_mov_b32 m0, s41
	ds_read_b128 v[188:191], v187 offset:16384
	ds_read_b128 v[192:195], v187 offset:17408
	ds_read_b128 v[196:199], v187 offset:18432
	ds_read_b128 v[200:203], v187 offset:19456
	ds_read_b128 v[204:207], v187 offset:20480
	ds_read_b128 v[208:211], v187 offset:21504
	ds_read_b128 v[212:215], v187 offset:22528
	ds_read_b128 v[216:219], v187 offset:23552
	global_load_lds_dwordx4 v[174:175], off
	s_add_i32 m0, s41, 0x2000
	s_add_u32 s50, s46, 0x40000
	v_lshl_add_u64 v[176:177], s[46:47], 0, v[162:163]
	s_addc_u32 s51, s47, 0
	s_add_i32 s41, s81, s56
	global_load_lds_dwordx4 v[176:177], off
	v_lshl_add_u64 v[178:179], s[50:51], 0, v[164:165]
	s_mov_b32 m0, s41
	v_lshl_add_u64 v[180:181], s[48:49], 0, v[168:169]
	global_load_lds_dwordx4 v[178:179], off
	v_lshl_add_u64 v[178:179], s[50:51], 0, v[162:163]
	s_add_i32 m0, s41, 0x2000
	s_nop 0
	global_load_lds_dwordx4 v[178:179], off
	v_lshl_add_u64 v[178:179], s[48:49], 0, v[166:167]
	s_mov_b32 m0, s1
	s_nop 0
	global_load_lds_dwordx4 v[178:179], off
	s_mov_b32 m0, s33
	s_nop 0
	global_load_lds_dwordx4 v[180:181], off
	s_cmp_eq_u32 s37, 12
	s_cbranch_scc1 .Lp10_wb
	s_waitcnt vmcnt(9)
.Lp10_wb:
	s_waitcnt vmcnt(13)
	s_waitcnt lgkmcnt(0)
	s_barrier
	s_setprio 1
	s_waitcnt lgkmcnt(0)
	v_mfma_f32_16x16x128_f8f6f4 v[94:97], v[18:25], v[188:195], v[94:97]
	v_mfma_f32_16x16x128_f8f6f4 v[90:93], v[26:33], v[188:195], v[90:93]
	v_mfma_f32_16x16x128_f8f6f4 v[78:81], v[18:25], v[196:203], v[78:81]
	v_mfma_f32_16x16x128_f8f6f4 v[66:69], v[26:33], v[196:203], v[66:69]
	v_mfma_f32_16x16x128_f8f6f4 v[50:53], v[18:25], v[204:211], v[50:53]
	v_mfma_f32_16x16x128_f8f6f4 v[46:49], v[26:33], v[204:211], v[46:49]
	v_mfma_f32_16x16x128_f8f6f4 v[38:41], v[18:25], v[212:219], v[38:41]
	v_mfma_f32_16x16x128_f8f6f4 v[34:37], v[26:33], v[212:219], v[34:37]
	s_setprio 0
	s_setprio 1
	v_mfma_f32_16x16x128_f8f6f4 v[82:85], v[2:9], v[188:195], v[82:85]
	v_mfma_f32_16x16x128_f8f6f4 v[70:73], v[10:17], v[188:195], v[70:73]
	v_mfma_f32_16x16x128_f8f6f4 v[54:57], v[2:9], v[196:203], v[54:57]
	v_mfma_f32_16x16x128_f8f6f4 v[42:45], v[10:17], v[196:203], v[42:45]
	v_mfma_f32_16x16x128_f8f6f4 v[74:77], v[2:9], v[204:211], v[74:77]
	v_mfma_f32_16x16x128_f8f6f4 v[86:89], v[10:17], v[204:211], v[86:89]
	v_mfma_f32_16x16x128_f8f6f4 v[58:61], v[2:9], v[212:219], v[58:61]
	v_mfma_f32_16x16x128_f8f6f4 v[62:65], v[10:17], v[212:219], v[62:65]
	s_setprio 0
	s_barrier
	s_add_i32 s41, 0, 0x18000
	s_add_i32 s50, 0, 0x1c000
	v_add_u32_e32 v14, s41, v182
	v_add_u32_e32 v30, 0x1000, v14
	ds_read_b128 v[2:5], v14
	ds_read_b128 v[6:9], v14 offset:1024
	ds_read_b128 v[10:13], v14 offset:2048
	ds_read_b128 v[14:17], v14 offset:3072
	ds_read_b128 v[18:21], v30
	ds_read_b128 v[22:25], v30 offset:1024
	ds_read_b128 v[26:29], v30 offset:2048
	ds_read_b128 v[30:33], v30 offset:3072
	s_mov_b32 m0, s54
	v_lshl_add_u64 v[220:221], s[48:49], 0, v[170:171]
	ds_read_b128 v[188:191], v187 offset:32768
	ds_read_b128 v[192:195], v187 offset:33792
	ds_read_b128 v[196:199], v187 offset:34816
	ds_read_b128 v[200:203], v187 offset:35840
	ds_read_b128 v[204:207], v187 offset:36864
	ds_read_b128 v[208:211], v187 offset:37888
	ds_read_b128 v[212:215], v187 offset:38912
	ds_read_b128 v[216:219], v187 offset:39936
	global_load_lds_dwordx4 v[220:221], off
	v_lshl_add_u64 v[220:221], s[48:49], 0, v[172:173]
	s_mov_b32 m0, s57
	s_nop 0
	global_load_lds_dwordx4 v[220:221], off
	s_cmp_eq_u32 s37, 12
	s_cbranch_scc1 .Lp10_wc
	s_waitcnt vmcnt(9)
.Lp10_wc:
	s_waitcnt vmcnt(13)
	s_waitcnt lgkmcnt(0)
	s_barrier
	s_setprio 1
	s_waitcnt lgkmcnt(0)
	v_mfma_f32_16x16x128_f8f6f4 v[158:161], v[2:9], v[188:195], v[158:161]
	v_mfma_f32_16x16x128_f8f6f4 v[154:157], v[10:17], v[188:195], v[154:157]
	v_mfma_f32_16x16x128_f8f6f4 v[150:153], v[2:9], v[196:203], v[150:153]
	v_mfma_f32_16x16x128_f8f6f4 v[146:149], v[10:17], v[196:203], v[146:149]
	v_mfma_f32_16x16x128_f8f6f4 v[142:145], v[2:9], v[204:211], v[142:145]
	v_mfma_f32_16x16x128_f8f6f4 v[134:137], v[10:17], v[204:211], v[134:137]
	v_mfma_f32_16x16x128_f8f6f4 v[118:121], v[2:9], v[212:219], v[118:121]
	v_mfma_f32_16x16x128_f8f6f4 v[110:113], v[10:17], v[212:219], v[110:113]
	s_setprio 0
	s_setprio 1
	v_mfma_f32_16x16x128_f8f6f4 v[138:141], v[18:25], v[188:195], v[138:141]
	v_mfma_f32_16x16x128_f8f6f4 v[130:133], v[26:33], v[188:195], v[130:133]
	v_mfma_f32_16x16x128_f8f6f4 v[126:129], v[18:25], v[196:203], v[126:129]
	v_mfma_f32_16x16x128_f8f6f4 v[122:125], v[26:33], v[196:203], v[122:125]
	v_mfma_f32_16x16x128_f8f6f4 v[114:117], v[18:25], v[204:211], v[114:117]
	v_mfma_f32_16x16x128_f8f6f4 v[106:109], v[26:33], v[204:211], v[106:109]
	v_mfma_f32_16x16x128_f8f6f4 v[102:105], v[18:25], v[212:219], v[102:105]
	v_mfma_f32_16x16x128_f8f6f4 v[98:101], v[26:33], v[212:219], v[98:101]
	s_setprio 0
	s_barrier
	s_add_i32 s41, s41, s56
	v_lshl_add_u64 v[174:175], v[174:175], 0, s[20:21]
	s_mov_b32 m0, s41
	ds_read_b128 v[188:191], v187 offset:49152
	ds_read_b128 v[192:195], v187 offset:50176
	ds_read_b128 v[196:199], v187 offset:51200
	ds_read_b128 v[200:203], v187 offset:52224
	ds_read_b128 v[204:207], v187 offset:53248
	ds_read_b128 v[208:211], v187 offset:54272
	ds_read_b128 v[212:215], v187 offset:55296
	ds_read_b128 v[216:219], v187 offset:56320
	global_load_lds_dwordx4 v[174:175], off
	s_add_i32 m0, s41, 0x2000
	s_add_u32 s46, s46, 0x40080
	v_lshl_add_u64 v[174:175], v[176:177], 0, s[20:21]
	s_addc_u32 s47, s47, 0
	s_add_i32 s41, s50, s56
	global_load_lds_dwordx4 v[174:175], off
	v_lshl_add_u64 v[174:175], s[46:47], 0, v[164:165]
	s_mov_b32 m0, s41
	s_nop 0
	global_load_lds_dwordx4 v[174:175], off
	v_lshl_add_u64 v[174:175], s[46:47], 0, v[162:163]
	s_add_i32 m0, s41, 0x2000
	s_nop 0
	global_load_lds_dwordx4 v[174:175], off
	v_lshl_add_u64 v[174:175], v[178:179], 0, s[20:21]
	s_mov_b32 m0, s60
	s_nop 0
	global_load_lds_dwordx4 v[174:175], off
	v_lshl_add_u64 v[174:175], v[180:181], 0, s[20:21]
	s_mov_b32 m0, s61
	s_nop 0
	global_load_lds_dwordx4 v[174:175], off
	s_waitcnt vmcnt(8)
	s_waitcnt lgkmcnt(0)
	s_barrier
	s_setprio 1
	s_waitcnt lgkmcnt(0)
	v_mfma_f32_16x16x128_f8f6f4 v[94:97], v[2:9], v[188:195], v[94:97]
	v_mfma_f32_16x16x128_f8f6f4 v[90:93], v[10:17], v[188:195], v[90:93]
	v_mfma_f32_16x16x128_f8f6f4 v[78:81], v[2:9], v[196:203], v[78:81]
	v_mfma_f32_16x16x128_f8f6f4 v[66:69], v[10:17], v[196:203], v[66:69]
	v_mfma_f32_16x16x128_f8f6f4 v[50:53], v[2:9], v[204:211], v[50:53]
	v_mfma_f32_16x16x128_f8f6f4 v[46:49], v[10:17], v[204:211], v[46:49]
	v_mfma_f32_16x16x128_f8f6f4 v[38:41], v[2:9], v[212:219], v[38:41]
	v_mfma_f32_16x16x128_f8f6f4 v[34:37], v[10:17], v[212:219], v[34:37]
	s_setprio 0
	s_setprio 1
	v_mfma_f32_16x16x128_f8f6f4 v[82:85], v[18:25], v[188:195], v[82:85]
	v_mfma_f32_16x16x128_f8f6f4 v[70:73], v[26:33], v[188:195], v[70:73]
	v_mfma_f32_16x16x128_f8f6f4 v[54:57], v[18:25], v[196:203], v[54:57]
	v_mfma_f32_16x16x128_f8f6f4 v[42:45], v[26:33], v[196:203], v[42:45]
	v_mfma_f32_16x16x128_f8f6f4 v[74:77], v[18:25], v[204:211], v[74:77]
	v_mfma_f32_16x16x128_f8f6f4 v[86:89], v[26:33], v[204:211], v[86:89]
	v_mfma_f32_16x16x128_f8f6f4 v[58:61], v[18:25], v[212:219], v[58:61]
	v_mfma_f32_16x16x128_f8f6f4 v[62:65], v[26:33], v[212:219], v[62:65]
	s_setprio 0
	s_barrier
	s_add_i32 s37, s37, 2
	s_cmp_gt_u32 s37, 13
	s_cbranch_scc0 .LBB0_1440
.LBB0_1443:
	s_mov_b32 s100, s85
	s_mov_b32 s101, 0
	s_lshl_b64 s[100:101], s[100:101], 19
	s_add_u32 s100, s100, s18
	s_addc_u32 s101, s101, s19
	s_lshl_b32 vcc_lo, s10, 8
	s_add_u32 s100, s100, vcc_lo
	s_addc_u32 s101, s101, 0
	s_ashr_i32 s41, s40, 31
	s_lshl_b64 s[40:41], s[40:41], 13
	v_lshl_or_b32 v20, s10, 8, v183
	s_add_u32 s40, s12, s40
	s_addc_u32 s41, s13, s41
	v_ashrrev_i32_e32 v21, 31, v20
	v_lshl_add_u64 v[2:3], v[20:21], 2, s[40:41]
	v_mov_b32_e32 v14, v238
	v_mov_b32_e32 v15, v239
	v_mov_b32_e32 v16, v240
	v_mov_b32_e32 v17, v241
	v_mov_b32_e32 v10, v242
	v_mov_b32_e32 v11, v243
	v_mov_b32_e32 v12, v244
	v_mov_b32_e32 v13, v245
	v_mov_b32_e32 v6, v246
	v_mov_b32_e32 v7, v247
	v_mov_b32_e32 v8, v248
	v_mov_b32_e32 v9, v249
	s_nop 0
	v_mov_b32_e32 v2, v250
	v_mov_b32_e32 v3, v251
	v_mov_b32_e32 v4, v252
	v_mov_b32_e32 v5, v253
	v_mov_b32_e32 v24, 0
	v_mov_b32_e32 v25, 0
	v_mov_b32_e32 v26, 0
	v_mov_b32_e32 v27, 0
	v_mov_b32_e32 v28, 0
	v_mov_b32_e32 v29, 0
	v_mov_b32_e32 v30, 0
	v_mov_b32_e32 v31, 0
	v_lshl_add_u32 v18, s85, 8, v1
	v_mov_b32_e32 v174, 0
	v_mov_b32_e32 v175, 0
	v_ashrrev_i32_e32 v19, 31, v18
	v_or_b32_e32 v22, 16, v18
	v_or_b32_e32 v176, 32, v18
	v_or_b32_e32 v178, 48, v18
	v_lshlrev_b64 v[18:19], 11, v[18:19]
	v_ashrrev_i32_e32 v23, 31, v22
	v_lshl_add_u64 v[18:19], s[18:19], 0, v[18:19]
	v_lshlrev_b64 v[22:23], 11, v[22:23]
	v_lshl_add_u64 v[18:19], v[18:19], 0, v[20:21]
	v_lshl_add_u64 v[22:23], s[18:19], 0, v[22:23]
	v_lshl_add_u64 v[180:181], v[22:23], 0, v[20:21]
	v_mov_b32_e32 v32, 0
	v_mov_b32_e32 v33, 0
	v_ashrrev_i32_e32 v177, 31, v176
	v_ashrrev_i32_e32 v179, 31, v178
	v_lshlrev_b64 v[176:177], 11, v[176:177]
	v_lshlrev_b64 v[178:179], 11, v[178:179]
	v_lshl_add_u64 v[176:177], s[18:19], 0, v[176:177]
	v_lshl_add_u64 v[178:179], s[18:19], 0, v[178:179]
	v_lshl_add_u64 v[176:177], v[176:177], 0, v[20:21]
	v_lshl_add_u64 v[178:179], v[178:179], 0, v[20:21]
	v_lshl_add_u64 v[188:189], v[18:19], 0, s[14:15]
	v_lshl_add_u64 v[190:191], v[18:19], 0, s[24:25]
	v_lshl_add_u64 v[22:23], v[18:19], 0, s[26:27]
	v_lshl_add_u64 v[20:21], v[18:19], 0, s[28:29]
	s_and_b64 vcc, exec, s[22:23]
	s_cbranch_vccz .Lp10_lbar
	s_barrier
.Lp10_lbar:
	s_nop 0
	v_pk_fma_f32 v[158:159], v[158:159], s[30:31], v[14:15] op_sel_hi:[1,0,1]
	v_pk_fma_f32 v[154:155], v[154:155], s[30:31], v[10:11] op_sel_hi:[1,0,1]
	v_pk_fma_f32 v[138:139], v[138:139], s[30:31], v[6:7] op_sel_hi:[1,0,1]
	v_pk_fma_f32 v[130:131], v[130:131], s[30:31], v[2:3] op_sel_hi:[1,0,1]
	v_cvt_pk_fp8_f32 v24, v158, v159
	v_cvt_pk_fp8_f32 v25, v154, v155
	v_pk_fma_f32 v[150:151], v[150:151], s[30:31], v[14:15] op_sel_hi:[1,0,1]
	v_pk_fma_f32 v[146:147], v[146:147], s[30:31], v[10:11] op_sel_hi:[1,0,1]
	v_cvt_pk_fp8_f32 v26, v138, v139
	v_cvt_pk_fp8_f32 v27, v130, v131
	v_pk_fma_f32 v[126:127], v[126:127], s[30:31], v[6:7] op_sel_hi:[1,0,1]
	v_pk_fma_f32 v[122:123], v[122:123], s[30:31], v[2:3] op_sel_hi:[1,0,1]
	v_cvt_pk_fp8_f32 v28, v150, v151
	v_cvt_pk_fp8_f32 v29, v146, v147
	v_pk_fma_f32 v[160:161], v[160:161], s[30:31], v[16:17] op_sel_hi:[1,0,1]
	v_pk_fma_f32 v[156:157], v[156:157], s[30:31], v[12:13] op_sel_hi:[1,0,1]
	v_cvt_pk_fp8_f32 v30, v126, v127
	v_cvt_pk_fp8_f32 v31, v122, v123
	v_pk_fma_f32 v[140:141], v[140:141], s[30:31], v[8:9] op_sel_hi:[1,0,1]
	v_pk_fma_f32 v[132:133], v[132:133], s[30:31], v[4:5] op_sel_hi:[1,0,1]
	v_pk_fma_f32 v[114:115], v[114:115], s[30:31], v[6:7] op_sel_hi:[1,0,1]
	v_pk_fma_f32 v[106:107], v[106:107], s[30:31], v[2:3] op_sel_hi:[1,0,1]
	v_cvt_pk_fp8_f32 v24, v160, v161 op_sel:[0,0,1]
	v_cvt_pk_fp8_f32 v25, v156, v157 op_sel:[0,0,1]
	v_pk_fma_f32 v[152:153], v[152:153], s[30:31], v[16:17] op_sel_hi:[1,0,1]
	v_pk_fma_f32 v[148:149], v[148:149], s[30:31], v[12:13] op_sel_hi:[1,0,1]
	v_cvt_pk_fp8_f32 v174, v114, v115
	v_cvt_pk_fp8_f32 v26, v140, v141 op_sel:[0,0,1]
	v_cvt_pk_fp8_f32 v27, v132, v133 op_sel:[0,0,1]
	v_cvt_pk_fp8_f32 v175, v106, v107
	v_pk_fma_f32 v[128:129], v[128:129], s[30:31], v[8:9] op_sel_hi:[1,0,1]
	v_pk_fma_f32 v[124:125], v[124:125], s[30:31], v[4:5] op_sel_hi:[1,0,1]
	v_cvt_pk_fp8_f32 v28, v152, v153 op_sel:[0,0,1]
	v_cvt_pk_fp8_f32 v29, v148, v149 op_sel:[0,0,1]
	v_cvt_pk_fp8_f32 v30, v128, v129 op_sel:[0,0,1]
	v_cvt_pk_fp8_f32 v31, v124, v125 op_sel:[0,0,1]
	v_mov_b32_e32 v222, v24
	v_mov_b32_e32 v223, v25
	v_mov_b32_e32 v224, v26
	v_mov_b32_e32 v225, v27
	s_nop 1
	v_permlane16_swap_b32 v222, v224
	v_permlane16_swap_b32 v223, v225
	v_mov_b32_e32 v226, v28
	v_mov_b32_e32 v227, v29
	v_mov_b32_e32 v228, v30
	v_mov_b32_e32 v229, v31
	s_nop 1
	v_permlane16_swap_b32 v226, v228
	v_permlane16_swap_b32 v227, v229
	v_pk_fma_f32 v[24:25], v[116:117], s[30:31], v[8:9] op_sel_hi:[1,0,1]
	v_pk_fma_f32 v[26:27], v[108:109], s[30:31], v[4:5] op_sel_hi:[1,0,1]
	v_cvt_pk_fp8_f32 v174, v24, v25 op_sel:[0,0,1]
	v_cvt_pk_fp8_f32 v175, v26, v27 op_sel:[0,0,1]
	v_pk_fma_f32 v[24:25], v[118:119], s[30:31], v[14:15] op_sel_hi:[1,0,1]
	v_pk_fma_f32 v[26:27], v[110:111], s[30:31], v[10:11] op_sel_hi:[1,0,1]
	v_mov_b32_e32 v28, 0
	v_mov_b32_e32 v29, 0
	v_cvt_pk_fp8_f32 v28, v24, v25
	v_cvt_pk_fp8_f32 v29, v26, v27
	v_pk_fma_f32 v[142:143], v[142:143], s[30:31], v[14:15] op_sel_hi:[1,0,1]
	v_pk_fma_f32 v[134:135], v[134:135], s[30:31], v[10:11] op_sel_hi:[1,0,1]
	v_cvt_pk_fp8_f32 v32, v142, v143
	v_cvt_pk_fp8_f32 v33, v134, v135
	v_pk_fma_f32 v[24:25], v[120:121], s[30:31], v[16:17] op_sel_hi:[1,0,1]
	v_pk_fma_f32 v[26:27], v[112:113], s[30:31], v[12:13] op_sel_hi:[1,0,1]
	v_cvt_pk_fp8_f32 v28, v24, v25 op_sel:[0,0,1]
	v_cvt_pk_fp8_f32 v29, v26, v27 op_sel:[0,0,1]
	v_pk_fma_f32 v[24:25], v[102:103], s[30:31], v[6:7] op_sel_hi:[1,0,1]
	v_pk_fma_f32 v[26:27], v[98:99], s[30:31], v[2:3] op_sel_hi:[1,0,1]
	v_mov_b32_e32 v30, 0
	v_mov_b32_e32 v31, 0
	v_pk_fma_f32 v[144:145], v[144:145], s[30:31], v[16:17] op_sel_hi:[1,0,1]
	v_pk_fma_f32 v[136:137], v[136:137], s[30:31], v[12:13] op_sel_hi:[1,0,1]
	v_cvt_pk_fp8_f32 v30, v24, v25
	v_cvt_pk_fp8_f32 v31, v26, v27
	v_cvt_pk_fp8_f32 v32, v144, v145 op_sel:[0,0,1]
	v_cvt_pk_fp8_f32 v33, v136, v137 op_sel:[0,0,1]
	v_pk_fma_f32 v[24:25], v[104:105], s[30:31], v[8:9] op_sel_hi:[1,0,1]
	v_pk_fma_f32 v[26:27], v[100:101], s[30:31], v[4:5] op_sel_hi:[1,0,1]
	v_cvt_pk_fp8_f32 v30, v24, v25 op_sel:[0,0,1]
	v_cvt_pk_fp8_f32 v31, v26, v27 op_sel:[0,0,1]
	v_mov_b32_e32 v230, v32
	v_mov_b32_e32 v231, v33
	v_mov_b32_e32 v232, v174
	v_mov_b32_e32 v233, v175
	s_nop 1
	v_permlane16_swap_b32 v230, v232
	v_permlane16_swap_b32 v231, v233
	v_mov_b32_e32 v234, v28
	v_mov_b32_e32 v235, v29
	v_mov_b32_e32 v236, v30
	v_mov_b32_e32 v237, v31
	s_nop 1
	v_permlane16_swap_b32 v234, v236
	v_permlane16_swap_b32 v235, v237
	v_pk_fma_f32 v[24:25], v[94:95], s[30:31], v[14:15] op_sel_hi:[1,0,1]
	v_pk_fma_f32 v[26:27], v[90:91], s[30:31], v[10:11] op_sel_hi:[1,0,1]
	v_mov_b32_e32 v28, 0
	v_mov_b32_e32 v29, 0
	v_cvt_pk_fp8_f32 v28, v24, v25
	v_cvt_pk_fp8_f32 v29, v26, v27
	v_pk_fma_f32 v[24:25], v[96:97], s[30:31], v[16:17] op_sel_hi:[1,0,1]
	v_pk_fma_f32 v[26:27], v[92:93], s[30:31], v[12:13] op_sel_hi:[1,0,1]
	v_cvt_pk_fp8_f32 v28, v24, v25 op_sel:[0,0,1]
	v_cvt_pk_fp8_f32 v29, v26, v27 op_sel:[0,0,1]
	v_pk_fma_f32 v[24:25], v[82:83], s[30:31], v[6:7] op_sel_hi:[1,0,1]
	v_pk_fma_f32 v[26:27], v[70:71], s[30:31], v[2:3] op_sel_hi:[1,0,1]
	v_mov_b32_e32 v30, 0
	v_mov_b32_e32 v31, 0
	v_cvt_pk_fp8_f32 v30, v24, v25
	v_cvt_pk_fp8_f32 v31, v26, v27
	v_pk_fma_f32 v[24:25], v[84:85], s[30:31], v[8:9] op_sel_hi:[1,0,1]
	v_pk_fma_f32 v[26:27], v[72:73], s[30:31], v[4:5] op_sel_hi:[1,0,1]
	v_cvt_pk_fp8_f32 v30, v24, v25 op_sel:[0,0,1]
	v_cvt_pk_fp8_f32 v31, v26, v27 op_sel:[0,0,1]
	v_add_co_u32_e32 v24, vcc, s58, v18
	v_pk_fma_f32 v[26:27], v[66:67], s[30:31], v[10:11] op_sel_hi:[1,0,1]
	s_nop 0
	v_addc_co_u32_e32 v25, vcc, 0, v19, vcc
	v_mov_b32_e32 v238, v28
	v_mov_b32_e32 v239, v29
	v_mov_b32_e32 v240, v30
	v_mov_b32_e32 v241, v31
	s_nop 1
	v_permlane16_swap_b32 v238, v240
	v_permlane16_swap_b32 v239, v241
	v_pk_fma_f32 v[24:25], v[78:79], s[30:31], v[14:15] op_sel_hi:[1,0,1]
	v_mov_b32_e32 v28, 0
	v_mov_b32_e32 v29, 0
	v_cvt_pk_fp8_f32 v28, v24, v25
	v_cvt_pk_fp8_f32 v29, v26, v27
	v_pk_fma_f32 v[24:25], v[80:81], s[30:31], v[16:17] op_sel_hi:[1,0,1]
	v_pk_fma_f32 v[26:27], v[68:69], s[30:31], v[12:13] op_sel_hi:[1,0,1]
	v_cvt_pk_fp8_f32 v28, v24, v25 op_sel:[0,0,1]
	v_cvt_pk_fp8_f32 v29, v26, v27 op_sel:[0,0,1]
	v_pk_fma_f32 v[24:25], v[54:55], s[30:31], v[6:7] op_sel_hi:[1,0,1]
	v_pk_fma_f32 v[26:27], v[42:43], s[30:31], v[2:3] op_sel_hi:[1,0,1]
	v_mov_b32_e32 v30, 0
	v_mov_b32_e32 v31, 0
	v_cvt_pk_fp8_f32 v30, v24, v25
	v_cvt_pk_fp8_f32 v31, v26, v27
	v_pk_fma_f32 v[24:25], v[56:57], s[30:31], v[8:9] op_sel_hi:[1,0,1]
	v_pk_fma_f32 v[26:27], v[44:45], s[30:31], v[4:5] op_sel_hi:[1,0,1]
	v_cvt_pk_fp8_f32 v30, v24, v25 op_sel:[0,0,1]
	v_cvt_pk_fp8_f32 v31, v26, v27 op_sel:[0,0,1]
	v_add_co_u32_e32 v24, vcc, s82, v18
	v_pk_fma_f32 v[26:27], v[46:47], s[30:31], v[10:11] op_sel_hi:[1,0,1]
	s_nop 0
	v_addc_co_u32_e32 v25, vcc, 0, v19, vcc
	v_mov_b32_e32 v242, v28
	v_mov_b32_e32 v243, v29
	v_mov_b32_e32 v244, v30
	v_mov_b32_e32 v245, v31
	s_nop 1
	v_permlane16_swap_b32 v242, v244
	v_permlane16_swap_b32 v243, v245
	v_pk_fma_f32 v[24:25], v[50:51], s[30:31], v[14:15] op_sel_hi:[1,0,1]
	v_mov_b32_e32 v28, 0
	v_mov_b32_e32 v29, 0
	v_cvt_pk_fp8_f32 v28, v24, v25
	v_cvt_pk_fp8_f32 v29, v26, v27
	v_pk_fma_f32 v[24:25], v[52:53], s[30:31], v[16:17] op_sel_hi:[1,0,1]
	v_pk_fma_f32 v[26:27], v[48:49], s[30:31], v[12:13] op_sel_hi:[1,0,1]
	v_cvt_pk_fp8_f32 v28, v24, v25 op_sel:[0,0,1]
	v_cvt_pk_fp8_f32 v29, v26, v27 op_sel:[0,0,1]
	v_pk_fma_f32 v[24:25], v[74:75], s[30:31], v[6:7] op_sel_hi:[1,0,1]
	v_pk_fma_f32 v[26:27], v[86:87], s[30:31], v[2:3] op_sel_hi:[1,0,1]
	v_mov_b32_e32 v30, 0
	v_mov_b32_e32 v31, 0
	v_cvt_pk_fp8_f32 v30, v24, v25
	v_cvt_pk_fp8_f32 v31, v26, v27
	v_pk_fma_f32 v[24:25], v[76:77], s[30:31], v[8:9] op_sel_hi:[1,0,1]
	v_pk_fma_f32 v[26:27], v[88:89], s[30:31], v[4:5] op_sel_hi:[1,0,1]
	v_cvt_pk_fp8_f32 v30, v24, v25 op_sel:[0,0,1]
	v_cvt_pk_fp8_f32 v31, v26, v27 op_sel:[0,0,1]
	v_add_co_u32_e32 v24, vcc, s83, v18
	v_pk_fma_f32 v[14:15], v[38:39], s[30:31], v[14:15] op_sel_hi:[1,0,1]
	s_nop 0
	v_addc_co_u32_e32 v25, vcc, 0, v19, vcc
	v_mov_b32_e32 v246, v28
	v_mov_b32_e32 v247, v29
	v_mov_b32_e32 v248, v30
	v_mov_b32_e32 v249, v31
	s_nop 1
	v_permlane16_swap_b32 v246, v248
	v_permlane16_swap_b32 v247, v249
	v_mov_b32_e32 v22, 0
	v_cvt_pk_fp8_f32 v22, v14, v15
	v_pk_fma_f32 v[10:11], v[34:35], s[30:31], v[10:11] op_sel_hi:[1,0,1]
	v_mov_b32_e32 v23, 0
	v_cvt_pk_fp8_f32 v23, v10, v11
	v_pk_fma_f32 v[10:11], v[40:41], s[30:31], v[16:17] op_sel_hi:[1,0,1]
	v_pk_fma_f32 v[6:7], v[58:59], s[30:31], v[6:7] op_sel_hi:[1,0,1]
	v_cvt_pk_fp8_f32 v22, v10, v11 op_sel:[0,0,1]
	v_pk_fma_f32 v[2:3], v[62:63], s[30:31], v[2:3] op_sel_hi:[1,0,1]
	v_mov_b32_e32 v10, 0
	v_mov_b32_e32 v11, 0
	v_cvt_pk_fp8_f32 v10, v6, v7
	v_cvt_pk_fp8_f32 v11, v2, v3
	v_pk_fma_f32 v[12:13], v[36:37], s[30:31], v[12:13] op_sel_hi:[1,0,1]
	v_pk_fma_f32 v[2:3], v[60:61], s[30:31], v[8:9] op_sel_hi:[1,0,1]
	v_cvt_pk_fp8_f32 v23, v12, v13 op_sel:[0,0,1]
	v_pk_fma_f32 v[4:5], v[64:65], s[30:31], v[4:5] op_sel_hi:[1,0,1]
	v_cvt_pk_fp8_f32 v10, v2, v3 op_sel:[0,0,1]
	v_cvt_pk_fp8_f32 v11, v4, v5 op_sel:[0,0,1]
	v_add_co_u32_e32 v2, vcc, s84, v18
	s_nop 1
	v_addc_co_u32_e32 v3, vcc, 0, v19, vcc
	s_andn2_b64 vcc, exec, s[6:7]
	s_mov_b64 s[6:7], -1
	v_mov_b32_e32 v250, v22
	v_mov_b32_e32 v251, v23
	v_mov_b32_e32 v252, v10
	v_mov_b32_e32 v253, v11
	s_nop 1
	v_permlane16_swap_b32 v250, v252
	v_permlane16_swap_b32 v251, v253
	s_cbranch_vccnz .LBB0_1434
	s_andn2_b64 vcc, exec, s[16:17]
	s_cbranch_vccnz .LBB0_1433
	s_barrier
	s_branch .LBB0_1433
